# MoE K loop: last iteration no longer issues the two clamped (redundant) prefetch steps; waits for everything instead
# speedup vs baseline: 1.0792x; 1.0069x over previous
.LBB0_3326:
	s_add_i32 s15, s16, 2
	s_add_i32 s16, s16, 4
	s_min_u32 s16, s16, 63
	s_mul_i32 s17, s14, 0xa000
	s_lshl_b32 s64, s16, 6
	s_add_i32 s20, s17, 0xffff6000
	s_cmp_lg_u32 s14, 0
	s_cselect_b32 s20, s20, 0x14000
	s_add_i32 s20, s18, s20
	s_waitcnt lgkmcnt(0)
	s_barrier
	s_cmp_lt_u32 s15, 62
	s_cbranch_scc0 .Lskipv_51971
	v_lshl_add_u64 v[156:157], v[202:203], 0, s[64:65]
	s_mov_b32 m0, s20
	s_nop 0
	global_load_lds_dwordx4 v[156:157], off
	v_lshl_add_u64 v[156:157], v[204:205], 0, s[64:65]
	s_add_i32 m0, s20, 0x400
	s_nop 0
	global_load_lds_dwordx4 v[156:157], off
	v_lshl_add_u64 v[156:157], v[206:207], 0, s[64:65]
	s_add_i32 m0, s20, 0x800
	s_nop 0
	global_load_lds_dwordx4 v[156:157], off
	v_lshl_add_u64 v[156:157], v[208:209], 0, s[64:65]
	s_add_i32 m0, s20, 0xc00
	s_nop 0
	global_load_lds_dwordx4 v[156:157], off
	v_lshl_add_u64 v[156:157], v[210:211], 0, s[64:65]
	s_add_i32 m0, s20, 0x1000
	s_lshl_b32 s64, s16, 16
	global_load_lds_dwordx4 v[156:157], off
	v_lshl_add_u64 v[160:161], v[212:213], 0, s[64:65]
	global_load_dwordx4 v[156:159], v[160:161], off nt
	s_nop 0
	global_load_dwordx4 v[160:163], v[160:161], off offset:2048 nt
.Lskipv_51971:
	v_add_u32_e32 v167, s17, v86
	ds_read2_b32 v[168:169], v201 offset0:0 offset1:0x84
	ds_read2_b32 v[170:171], v232 offset0:0 offset1:0x84
	ds_read2_b32 v[172:173], v201 offset0:16 offset1:0x94
	ds_read2_b32 v[174:175], v232 offset0:16 offset1:0x94
	ds_read2_b32 v[176:177], v201 offset0:32 offset1:0xa4
	ds_read2_b32 v[178:179], v232 offset0:32 offset1:0xa4
	ds_read2_b32 v[180:181], v201 offset0:48 offset1:0xb4
	ds_read2_b32 v[182:183], v232 offset0:48 offset1:0xb4
	ds_read_b128 v[184:187], v167 offset:0
	ds_read_b128 v[188:191], v167 offset:0x400
	s_nop 0
	s_waitcnt lgkmcnt(1)
	s_setprio 1
	v_mfma_f32_16x16x32_bf16 v[140:143], v[168:171], v[184:187], v[140:143]
	v_mfma_f32_16x16x32_bf16 v[132:135], v[172:175], v[184:187], v[132:135]
	v_mfma_f32_16x16x32_bf16 v[144:147], v[176:179], v[184:187], v[144:147]
	v_mfma_f32_16x16x32_bf16 v[136:139], v[180:183], v[184:187], v[136:139]
	ds_read_b128 v[184:187], v167 offset:0x800
	s_waitcnt lgkmcnt(1)
	s_nop 0
	v_mfma_f32_16x16x32_bf16 v[124:127], v[168:171], v[188:191], v[124:127]
	v_mfma_f32_16x16x32_bf16 v[112:115], v[172:175], v[188:191], v[112:115]
	v_mfma_f32_16x16x32_bf16 v[128:131], v[176:179], v[188:191], v[128:131]
	v_mfma_f32_16x16x32_bf16 v[116:119], v[180:183], v[188:191], v[116:119]
	ds_read_b128 v[188:191], v167 offset:0xc00
	s_waitcnt lgkmcnt(1)
	s_nop 0
	v_mfma_f32_16x16x32_bf16 v[82:85], v[168:171], v[184:187], v[82:85]
	v_mfma_f32_16x16x32_bf16 v[54:57], v[172:175], v[184:187], v[54:57]
	v_mfma_f32_16x16x32_bf16 v[88:91], v[176:179], v[184:187], v[88:91]
	v_mfma_f32_16x16x32_bf16 v[58:61], v[180:183], v[184:187], v[58:61]
	ds_read_b128 v[184:187], v167 offset:0x1000
	s_waitcnt lgkmcnt(1)
	s_nop 0
	v_mfma_f32_16x16x32_bf16 v[26:29], v[168:171], v[188:191], v[26:29]
	v_mfma_f32_16x16x32_bf16 v[6:9], v[172:175], v[188:191], v[6:9]
	v_mfma_f32_16x16x32_bf16 v[42:45], v[176:179], v[188:191], v[42:45]
	v_mfma_f32_16x16x32_bf16 v[14:17], v[180:183], v[188:191], v[14:17]
	ds_read_b128 v[188:191], v167 offset:0x1400
	s_waitcnt lgkmcnt(1)
	s_nop 0
	v_mfma_f32_16x16x32_bf16 v[92:95], v[168:171], v[184:187], v[92:95]
	v_mfma_f32_16x16x32_bf16 v[62:65], v[172:175], v[184:187], v[62:65]
	v_mfma_f32_16x16x32_bf16 v[96:99], v[176:179], v[184:187], v[96:99]
	v_mfma_f32_16x16x32_bf16 v[66:69], v[180:183], v[184:187], v[66:69]
	ds_read_b128 v[184:187], v167 offset:0x1800
	s_waitcnt lgkmcnt(1)
	s_nop 0
	v_mfma_f32_16x16x32_bf16 v[38:41], v[168:171], v[188:191], v[38:41]
	v_mfma_f32_16x16x32_bf16 v[18:21], v[172:175], v[188:191], v[18:21]
	v_mfma_f32_16x16x32_bf16 v[46:49], v[176:179], v[188:191], v[46:49]
	v_mfma_f32_16x16x32_bf16 v[22:25], v[180:183], v[188:191], v[22:25]
	ds_read_b128 v[188:191], v167 offset:0x1c00
	s_waitcnt lgkmcnt(1)
	s_nop 0
	v_mfma_f32_16x16x32_bf16 v[108:111], v[168:171], v[184:187], v[108:111]
	s_waitcnt lgkmcnt(0)
	v_mfma_f32_16x16x32_bf16 v[100:103], v[172:175], v[184:187], v[100:103]
	v_mfma_f32_16x16x32_bf16 v[120:123], v[176:179], v[184:187], v[120:123]
	v_mfma_f32_16x16x32_bf16 v[104:107], v[180:183], v[184:187], v[104:107]
	v_mfma_f32_16x16x32_bf16 v[70:73], v[168:171], v[188:191], v[70:73]
	v_mfma_f32_16x16x32_bf16 v[50:53], v[172:175], v[188:191], v[50:53]
	v_mfma_f32_16x16x32_bf16 v[10:13], v[176:179], v[188:191], v[10:13]
	v_mfma_f32_16x16x32_bf16 v[2:5], v[180:183], v[188:191], v[2:5]
	s_setprio 0
	s_cmp_lt_u32 s15, 62
	s_cbranch_scc1 .Lokw_51971
	s_waitcnt vmcnt(0)
.Lokw_51971:
	s_add_i32 s16, s14, 1
	s_cmp_lg_u32 s14, 2
	s_cselect_b32 s14, s16, 0
	s_min_u32 s16, s15, 60
	s_add_i32 s16, s16, 3
	s_mul_i32 s17, s14, 0xa000
	s_lshl_b32 s64, s16, 6
	s_add_i32 s20, s17, 0xffff6000
	s_cmp_lg_u32 s14, 0
	s_waitcnt vmcnt(7)
	v_cvt_pk_bf16_f32 v148, v152, v148
	v_add_u32_e32 v152, 0x20100, v165
	s_cselect_b32 s20, s20, 0x14000
	v_cvt_pk_bf16_f32 v149, v153, v149
	v_cvt_pk_bf16_f32 v150, v154, v150
	v_cvt_pk_bf16_f32 v151, v155, v151
	ds_write_b128 v152, v[148:151]
	v_lshl_add_u64 v[168:169], v[202:203], 0, s[64:65]
	v_lshl_add_u64 v[170:171], v[204:205], 0, s[64:65]
	v_lshl_add_u64 v[172:173], v[206:207], 0, s[64:65]
	v_lshl_add_u64 v[174:175], v[208:209], 0, s[64:65]
	v_lshl_add_u64 v[176:177], v[210:211], 0, s[64:65]
	s_lshl_b32 s64, s16, 16
	s_add_i32 s16, s18, s20
	s_waitcnt lgkmcnt(0)
	s_barrier
	s_cmp_lt_u32 s15, 62
	s_cbranch_scc0 .Lskipv_52148
	v_lshl_add_u64 v[148:149], v[212:213], 0, s[64:65]
	s_mov_b32 m0, s16
	global_load_dwordx4 v[152:155], v[148:149], off nt
	s_nop 0
	global_load_dwordx4 v[148:151], v[148:149], off offset:2048 nt
	s_nop 0
	global_load_lds_dwordx4 v[168:169], off
	s_add_i32 m0, s16, 0x400
	s_nop 0
	global_load_lds_dwordx4 v[170:171], off
	s_add_i32 m0, s16, 0x800
	s_nop 0
	global_load_lds_dwordx4 v[172:173], off
	s_add_i32 m0, s16, 0xc00
	s_nop 0
	global_load_lds_dwordx4 v[174:175], off
	s_add_i32 m0, s16, 0x1000
	s_nop 0
	global_load_lds_dwordx4 v[176:177], off
.Lskipv_52148:
	v_add_u32_e32 v167, s17, v86
	ds_read2_b32 v[168:169], v233 offset0:0 offset1:0x84
	ds_read2_b32 v[170:171], v234 offset0:0 offset1:0x84
	ds_read2_b32 v[172:173], v233 offset0:16 offset1:0x94
	ds_read2_b32 v[174:175], v234 offset0:16 offset1:0x94
	ds_read2_b32 v[176:177], v233 offset0:32 offset1:0xa4
	ds_read2_b32 v[178:179], v234 offset0:32 offset1:0xa4
	ds_read2_b32 v[180:181], v233 offset0:48 offset1:0xb4
	ds_read2_b32 v[182:183], v234 offset0:48 offset1:0xb4
	ds_read_b128 v[184:187], v167 offset:0
	ds_read_b128 v[188:191], v167 offset:0x400
	s_nop 0
	s_waitcnt lgkmcnt(1)
	s_setprio 1
	v_mfma_f32_16x16x32_bf16 v[140:143], v[168:171], v[184:187], v[140:143]
	v_mfma_f32_16x16x32_bf16 v[132:135], v[172:175], v[184:187], v[132:135]
	v_mfma_f32_16x16x32_bf16 v[144:147], v[176:179], v[184:187], v[144:147]
	v_mfma_f32_16x16x32_bf16 v[136:139], v[180:183], v[184:187], v[136:139]
	ds_read_b128 v[184:187], v167 offset:0x800
	s_waitcnt lgkmcnt(1)
	s_nop 0
	v_mfma_f32_16x16x32_bf16 v[124:127], v[168:171], v[188:191], v[124:127]
	v_mfma_f32_16x16x32_bf16 v[112:115], v[172:175], v[188:191], v[112:115]
	v_mfma_f32_16x16x32_bf16 v[128:131], v[176:179], v[188:191], v[128:131]
	v_mfma_f32_16x16x32_bf16 v[116:119], v[180:183], v[188:191], v[116:119]
	ds_read_b128 v[188:191], v167 offset:0xc00
	s_waitcnt lgkmcnt(1)
	s_nop 0
	v_mfma_f32_16x16x32_bf16 v[82:85], v[168:171], v[184:187], v[82:85]
	v_mfma_f32_16x16x32_bf16 v[54:57], v[172:175], v[184:187], v[54:57]
	v_mfma_f32_16x16x32_bf16 v[88:91], v[176:179], v[184:187], v[88:91]
	v_mfma_f32_16x16x32_bf16 v[58:61], v[180:183], v[184:187], v[58:61]
	ds_read_b128 v[184:187], v167 offset:0x1000
	s_waitcnt lgkmcnt(1)
	s_nop 0
	v_mfma_f32_16x16x32_bf16 v[26:29], v[168:171], v[188:191], v[26:29]
	v_mfma_f32_16x16x32_bf16 v[6:9], v[172:175], v[188:191], v[6:9]
	v_mfma_f32_16x16x32_bf16 v[42:45], v[176:179], v[188:191], v[42:45]
	v_mfma_f32_16x16x32_bf16 v[14:17], v[180:183], v[188:191], v[14:17]
	ds_read_b128 v[188:191], v167 offset:0x1400
	s_waitcnt lgkmcnt(1)
	s_nop 0
	v_mfma_f32_16x16x32_bf16 v[92:95], v[168:171], v[184:187], v[92:95]
	v_mfma_f32_16x16x32_bf16 v[62:65], v[172:175], v[184:187], v[62:65]
	v_mfma_f32_16x16x32_bf16 v[96:99], v[176:179], v[184:187], v[96:99]
	v_mfma_f32_16x16x32_bf16 v[66:69], v[180:183], v[184:187], v[66:69]
	ds_read_b128 v[184:187], v167 offset:0x1800
	s_waitcnt lgkmcnt(1)
	s_nop 0
	v_mfma_f32_16x16x32_bf16 v[38:41], v[168:171], v[188:191], v[38:41]
	v_mfma_f32_16x16x32_bf16 v[18:21], v[172:175], v[188:191], v[18:21]
	v_mfma_f32_16x16x32_bf16 v[46:49], v[176:179], v[188:191], v[46:49]
	v_mfma_f32_16x16x32_bf16 v[22:25], v[180:183], v[188:191], v[22:25]
	ds_read_b128 v[188:191], v167 offset:0x1c00
	s_waitcnt lgkmcnt(1)
	s_nop 0
	v_mfma_f32_16x16x32_bf16 v[108:111], v[168:171], v[184:187], v[108:111]
	s_waitcnt lgkmcnt(0)
	v_mfma_f32_16x16x32_bf16 v[100:103], v[172:175], v[184:187], v[100:103]
	v_mfma_f32_16x16x32_bf16 v[120:123], v[176:179], v[184:187], v[120:123]
	v_mfma_f32_16x16x32_bf16 v[104:107], v[180:183], v[184:187], v[104:107]
	v_mfma_f32_16x16x32_bf16 v[70:73], v[168:171], v[188:191], v[70:73]
	v_mfma_f32_16x16x32_bf16 v[50:53], v[172:175], v[188:191], v[50:53]
	v_mfma_f32_16x16x32_bf16 v[10:13], v[176:179], v[188:191], v[10:13]
	v_mfma_f32_16x16x32_bf16 v[2:5], v[180:183], v[188:191], v[2:5]
	s_setprio 0
	s_cmp_lt_u32 s15, 62
	s_cbranch_scc1 .Lokw_52148
	s_waitcnt vmcnt(0)
.Lokw_52148:
	s_waitcnt vmcnt(7)
	s_add_i32 s16, s14, 1
	s_cmp_lg_u32 s14, 2
	s_cselect_b32 s14, s16, 0
	s_cmp_gt_u32 s15, 61
	s_mov_b32 s16, s15
	s_waitcnt vmcnt(7)
	v_cvt_pk_bf16_f32 v156, v156, v160
	v_cvt_pk_bf16_f32 v157, v157, v161
	v_cvt_pk_bf16_f32 v158, v158, v162
	v_cvt_pk_bf16_f32 v159, v159, v163
	ds_write_b128 v166, v[156:159]
	s_cbranch_scc0 .LBB0_3326
	s_waitcnt vmcnt(0)
	s_mov_b64 s[14:15], 0
	s_branch .LBB0_3333

.LBB0_3344:
	s_add_i32 s13, s14, 2
	s_add_i32 s14, s14, 4
	s_min_u32 s14, s14, 63
	s_mul_i32 s15, s12, 0xa000
	s_lshl_b32 s64, s14, 6
	s_add_i32 s16, s15, 0xffff6000
	s_cmp_lg_u32 s12, 0
	s_cselect_b32 s16, s16, 0x14000
	s_add_i32 s16, s18, s16
	s_waitcnt lgkmcnt(0)
	s_barrier
	s_cmp_lt_u32 s13, 62
	s_cbranch_scc0 .Lskipv_53495
	v_lshl_add_u64 v[188:189], v[202:203], 0, s[64:65]
	s_mov_b32 m0, s16
	s_nop 0
	global_load_lds_dwordx4 v[188:189], off
	v_lshl_add_u64 v[188:189], v[204:205], 0, s[64:65]
	s_add_i32 m0, s16, 0x400
	s_nop 0
	global_load_lds_dwordx4 v[188:189], off
	v_lshl_add_u64 v[188:189], v[206:207], 0, s[64:65]
	s_add_i32 m0, s16, 0x800
	s_nop 0
	global_load_lds_dwordx4 v[188:189], off
	v_lshl_add_u64 v[188:189], v[208:209], 0, s[64:65]
	s_add_i32 m0, s16, 0xc00
	s_nop 0
	global_load_lds_dwordx4 v[188:189], off
	v_lshl_add_u64 v[188:189], v[210:211], 0, s[64:65]
	s_add_i32 m0, s16, 0x1000
	s_lshl_b32 s64, s14, 16
	global_load_lds_dwordx4 v[188:189], off
	v_lshl_add_u64 v[192:193], v[212:213], 0, s[64:65]
	global_load_dwordx4 v[188:191], v[192:193], off nt
	s_nop 0
	global_load_dwordx4 v[192:195], v[192:193], off offset:2048 nt
.Lskipv_53495:
	v_add_u32_e32 v216, s15, v86
	ds_read2_b32 v[196:197], v201 offset0:0 offset1:0x84
	ds_read2_b32 v[198:199], v232 offset0:0 offset1:0x84
	ds_read2_b32 v[222:223], v201 offset0:16 offset1:0x94
	ds_read2_b32 v[224:225], v232 offset0:16 offset1:0x94
	ds_read2_b32 v[226:227], v201 offset0:32 offset1:0xa4
	ds_read2_b32 v[228:229], v232 offset0:32 offset1:0xa4
	ds_read2_b32 v[238:239], v201 offset0:48 offset1:0xb4
	ds_read2_b32 v[240:241], v232 offset0:48 offset1:0xb4
	ds_read_b128 v[242:245], v216 offset:0
	ds_read_b128 v[246:249], v216 offset:0x400
	s_nop 0
	s_waitcnt lgkmcnt(1)
	s_setprio 1
	v_mfma_f32_16x16x32_bf16 v[140:143], v[196:199], v[242:245], v[140:143]
	v_mfma_f32_16x16x32_bf16 v[132:135], v[222:225], v[242:245], v[132:135]
	v_mfma_f32_16x16x32_bf16 v[144:147], v[226:229], v[242:245], v[144:147]
	v_mfma_f32_16x16x32_bf16 v[136:139], v[238:241], v[242:245], v[136:139]
	ds_read_b128 v[242:245], v216 offset:0x800
	s_waitcnt lgkmcnt(1)
	s_nop 0
	v_mfma_f32_16x16x32_bf16 v[124:127], v[196:199], v[246:249], v[124:127]
	v_mfma_f32_16x16x32_bf16 v[112:115], v[222:225], v[246:249], v[112:115]
	v_mfma_f32_16x16x32_bf16 v[128:131], v[226:229], v[246:249], v[128:131]
	v_mfma_f32_16x16x32_bf16 v[116:119], v[238:241], v[246:249], v[116:119]
	ds_read_b128 v[246:249], v216 offset:0xc00
	s_waitcnt lgkmcnt(1)
	s_nop 0
	v_mfma_f32_16x16x32_bf16 v[82:85], v[196:199], v[242:245], v[82:85]
	v_mfma_f32_16x16x32_bf16 v[54:57], v[222:225], v[242:245], v[54:57]
	v_mfma_f32_16x16x32_bf16 v[88:91], v[226:229], v[242:245], v[88:91]
	v_mfma_f32_16x16x32_bf16 v[58:61], v[238:241], v[242:245], v[58:61]
	ds_read_b128 v[242:245], v216 offset:0x1000
	s_waitcnt lgkmcnt(1)
	s_nop 0
	v_mfma_f32_16x16x32_bf16 v[26:29], v[196:199], v[246:249], v[26:29]
	v_mfma_f32_16x16x32_bf16 v[6:9], v[222:225], v[246:249], v[6:9]
	v_mfma_f32_16x16x32_bf16 v[42:45], v[226:229], v[246:249], v[42:45]
	v_mfma_f32_16x16x32_bf16 v[14:17], v[238:241], v[246:249], v[14:17]
	ds_read_b128 v[246:249], v216 offset:0x1400
	s_waitcnt lgkmcnt(1)
	s_nop 0
	v_mfma_f32_16x16x32_bf16 v[92:95], v[196:199], v[242:245], v[92:95]
	v_mfma_f32_16x16x32_bf16 v[62:65], v[222:225], v[242:245], v[62:65]
	v_mfma_f32_16x16x32_bf16 v[96:99], v[226:229], v[242:245], v[96:99]
	v_mfma_f32_16x16x32_bf16 v[66:69], v[238:241], v[242:245], v[66:69]
	ds_read_b128 v[242:245], v216 offset:0x1800
	s_waitcnt lgkmcnt(1)
	s_nop 0
	v_mfma_f32_16x16x32_bf16 v[38:41], v[196:199], v[246:249], v[38:41]
	v_mfma_f32_16x16x32_bf16 v[18:21], v[222:225], v[246:249], v[18:21]
	v_mfma_f32_16x16x32_bf16 v[46:49], v[226:229], v[246:249], v[46:49]
	v_mfma_f32_16x16x32_bf16 v[22:25], v[238:241], v[246:249], v[22:25]
	ds_read_b128 v[246:249], v216 offset:0x1c00
	s_waitcnt lgkmcnt(1)
	s_nop 0
	v_mfma_f32_16x16x32_bf16 v[108:111], v[196:199], v[242:245], v[108:111]
	v_mfma_f32_16x16x32_bf16 v[100:103], v[222:225], v[242:245], v[100:103]
	v_mfma_f32_16x16x32_bf16 v[120:123], v[226:229], v[242:245], v[120:123]
	v_mfma_f32_16x16x32_bf16 v[104:107], v[238:241], v[242:245], v[104:107]
	ds_read_b128 v[242:245], v216 offset:0x2000
	s_waitcnt lgkmcnt(1)
	s_nop 0
	v_mfma_f32_16x16x32_bf16 v[70:73], v[196:199], v[246:249], v[70:73]
	v_mfma_f32_16x16x32_bf16 v[50:53], v[222:225], v[246:249], v[50:53]
	v_mfma_f32_16x16x32_bf16 v[10:13], v[226:229], v[246:249], v[10:13]
	v_mfma_f32_16x16x32_bf16 v[2:5], v[238:241], v[246:249], v[2:5]
	ds_read_b128 v[246:249], v216 offset:0x2400
	s_waitcnt lgkmcnt(1)
	s_nop 0
	v_mfma_f32_16x16x32_bf16 v[176:179], v[196:199], v[242:245], v[176:179]
	s_waitcnt lgkmcnt(0)
	v_mfma_f32_16x16x32_bf16 v[168:171], v[222:225], v[242:245], v[168:171]
	v_mfma_f32_16x16x32_bf16 v[172:175], v[226:229], v[242:245], v[172:175]
	v_mfma_f32_16x16x32_bf16 v[164:167], v[238:241], v[242:245], v[164:167]
	v_mfma_f32_16x16x32_bf16 v[160:163], v[196:199], v[246:249], v[160:163]
	v_mfma_f32_16x16x32_bf16 v[152:155], v[222:225], v[246:249], v[152:155]
	v_mfma_f32_16x16x32_bf16 v[156:159], v[226:229], v[246:249], v[156:159]
	v_mfma_f32_16x16x32_bf16 v[148:151], v[238:241], v[246:249], v[148:151]
	s_setprio 0
	s_cmp_lt_u32 s13, 62
	s_cbranch_scc1 .Lokw_53495
	s_waitcnt vmcnt(0)
.Lokw_53495:
	s_add_i32 s14, s12, 1
	s_cmp_lg_u32 s12, 2
	s_cselect_b32 s12, s14, 0
	s_min_u32 s14, s13, 60
	s_add_i32 s14, s14, 3
	s_mul_i32 s15, s12, 0xa000
	s_lshl_b32 s64, s14, 6
	s_add_i32 s16, s15, 0xffff6000
	s_cmp_lg_u32 s12, 0
	s_waitcnt vmcnt(7)
	v_cvt_pk_bf16_f32 v180, v184, v180
	v_add_u32_e32 v184, 0x20100, v235
	s_cselect_b32 s16, s16, 0x14000
	v_cvt_pk_bf16_f32 v181, v185, v181
	v_cvt_pk_bf16_f32 v182, v186, v182
	v_cvt_pk_bf16_f32 v183, v187, v183
	ds_write_b128 v184, v[180:183]
	v_lshl_add_u64 v[196:197], v[202:203], 0, s[64:65]
	v_lshl_add_u64 v[198:199], v[204:205], 0, s[64:65]
	v_lshl_add_u64 v[216:217], v[206:207], 0, s[64:65]
	v_lshl_add_u64 v[222:223], v[208:209], 0, s[64:65]
	v_lshl_add_u64 v[224:225], v[210:211], 0, s[64:65]
	s_lshl_b32 s64, s14, 16
	s_add_i32 s14, s18, s16
	s_waitcnt lgkmcnt(0)
	s_barrier
	s_cmp_lt_u32 s13, 62
	s_cbranch_scc0 .Lskipv_53694
	v_lshl_add_u64 v[180:181], v[212:213], 0, s[64:65]
	s_mov_b32 m0, s14
	global_load_dwordx4 v[184:187], v[180:181], off nt
	s_nop 0
	global_load_dwordx4 v[180:183], v[180:181], off offset:2048 nt
	s_nop 0
	global_load_lds_dwordx4 v[196:197], off
	s_add_i32 m0, s14, 0x400
	s_nop 0
	global_load_lds_dwordx4 v[198:199], off
	s_add_i32 m0, s14, 0x800
	s_nop 0
	global_load_lds_dwordx4 v[216:217], off
	s_add_i32 m0, s14, 0xc00
	s_nop 0
	global_load_lds_dwordx4 v[222:223], off
	s_add_i32 m0, s14, 0x1000
	s_nop 0
	global_load_lds_dwordx4 v[224:225], off
.Lskipv_53694:
	v_add_u32_e32 v216, s15, v86
	ds_read2_b32 v[196:197], v233 offset0:0 offset1:0x84
	ds_read2_b32 v[198:199], v234 offset0:0 offset1:0x84
	ds_read2_b32 v[222:223], v233 offset0:16 offset1:0x94
	ds_read2_b32 v[224:225], v234 offset0:16 offset1:0x94
	ds_read2_b32 v[226:227], v233 offset0:32 offset1:0xa4
	ds_read2_b32 v[228:229], v234 offset0:32 offset1:0xa4
	ds_read2_b32 v[238:239], v233 offset0:48 offset1:0xb4
	ds_read2_b32 v[240:241], v234 offset0:48 offset1:0xb4
	ds_read_b128 v[242:245], v216 offset:0
	ds_read_b128 v[246:249], v216 offset:0x400
	s_nop 0
	s_waitcnt lgkmcnt(1)
	s_setprio 1
	v_mfma_f32_16x16x32_bf16 v[140:143], v[196:199], v[242:245], v[140:143]
	v_mfma_f32_16x16x32_bf16 v[132:135], v[222:225], v[242:245], v[132:135]
	v_mfma_f32_16x16x32_bf16 v[144:147], v[226:229], v[242:245], v[144:147]
	v_mfma_f32_16x16x32_bf16 v[136:139], v[238:241], v[242:245], v[136:139]
	ds_read_b128 v[242:245], v216 offset:0x800
	s_waitcnt lgkmcnt(1)
	s_nop 0
	v_mfma_f32_16x16x32_bf16 v[124:127], v[196:199], v[246:249], v[124:127]
	v_mfma_f32_16x16x32_bf16 v[112:115], v[222:225], v[246:249], v[112:115]
	v_mfma_f32_16x16x32_bf16 v[128:131], v[226:229], v[246:249], v[128:131]
	v_mfma_f32_16x16x32_bf16 v[116:119], v[238:241], v[246:249], v[116:119]
	ds_read_b128 v[246:249], v216 offset:0xc00
	s_waitcnt lgkmcnt(1)
	s_nop 0
	v_mfma_f32_16x16x32_bf16 v[82:85], v[196:199], v[242:245], v[82:85]
	v_mfma_f32_16x16x32_bf16 v[54:57], v[222:225], v[242:245], v[54:57]
	v_mfma_f32_16x16x32_bf16 v[88:91], v[226:229], v[242:245], v[88:91]
	v_mfma_f32_16x16x32_bf16 v[58:61], v[238:241], v[242:245], v[58:61]
	ds_read_b128 v[242:245], v216 offset:0x1000
	s_waitcnt lgkmcnt(1)
	s_nop 0
	v_mfma_f32_16x16x32_bf16 v[26:29], v[196:199], v[246:249], v[26:29]
	v_mfma_f32_16x16x32_bf16 v[6:9], v[222:225], v[246:249], v[6:9]
	v_mfma_f32_16x16x32_bf16 v[42:45], v[226:229], v[246:249], v[42:45]
	v_mfma_f32_16x16x32_bf16 v[14:17], v[238:241], v[246:249], v[14:17]
	ds_read_b128 v[246:249], v216 offset:0x1400
	s_waitcnt lgkmcnt(1)
	s_nop 0
	v_mfma_f32_16x16x32_bf16 v[92:95], v[196:199], v[242:245], v[92:95]
	v_mfma_f32_16x16x32_bf16 v[62:65], v[222:225], v[242:245], v[62:65]
	v_mfma_f32_16x16x32_bf16 v[96:99], v[226:229], v[242:245], v[96:99]
	v_mfma_f32_16x16x32_bf16 v[66:69], v[238:241], v[242:245], v[66:69]
	ds_read_b128 v[242:245], v216 offset:0x1800
	s_waitcnt lgkmcnt(1)
	s_nop 0
	v_mfma_f32_16x16x32_bf16 v[38:41], v[196:199], v[246:249], v[38:41]
	v_mfma_f32_16x16x32_bf16 v[18:21], v[222:225], v[246:249], v[18:21]
	v_mfma_f32_16x16x32_bf16 v[46:49], v[226:229], v[246:249], v[46:49]
	v_mfma_f32_16x16x32_bf16 v[22:25], v[238:241], v[246:249], v[22:25]
	ds_read_b128 v[246:249], v216 offset:0x1c00
	s_waitcnt lgkmcnt(1)
	s_nop 0
	v_mfma_f32_16x16x32_bf16 v[108:111], v[196:199], v[242:245], v[108:111]
	v_mfma_f32_16x16x32_bf16 v[100:103], v[222:225], v[242:245], v[100:103]
	v_mfma_f32_16x16x32_bf16 v[120:123], v[226:229], v[242:245], v[120:123]
	v_mfma_f32_16x16x32_bf16 v[104:107], v[238:241], v[242:245], v[104:107]
	ds_read_b128 v[242:245], v216 offset:0x2000
	s_waitcnt lgkmcnt(1)
	s_nop 0
	v_mfma_f32_16x16x32_bf16 v[70:73], v[196:199], v[246:249], v[70:73]
	v_mfma_f32_16x16x32_bf16 v[50:53], v[222:225], v[246:249], v[50:53]
	v_mfma_f32_16x16x32_bf16 v[10:13], v[226:229], v[246:249], v[10:13]
	v_mfma_f32_16x16x32_bf16 v[2:5], v[238:241], v[246:249], v[2:5]
	ds_read_b128 v[246:249], v216 offset:0x2400
	s_waitcnt lgkmcnt(1)
	s_nop 0
	v_mfma_f32_16x16x32_bf16 v[176:179], v[196:199], v[242:245], v[176:179]
	s_waitcnt lgkmcnt(0)
	v_mfma_f32_16x16x32_bf16 v[168:171], v[222:225], v[242:245], v[168:171]
	v_mfma_f32_16x16x32_bf16 v[172:175], v[226:229], v[242:245], v[172:175]
	v_mfma_f32_16x16x32_bf16 v[164:167], v[238:241], v[242:245], v[164:167]
	v_mfma_f32_16x16x32_bf16 v[160:163], v[196:199], v[246:249], v[160:163]
	v_mfma_f32_16x16x32_bf16 v[152:155], v[222:225], v[246:249], v[152:155]
	v_mfma_f32_16x16x32_bf16 v[156:159], v[226:229], v[246:249], v[156:159]
	v_mfma_f32_16x16x32_bf16 v[148:151], v[238:241], v[246:249], v[148:151]
	s_setprio 0
	s_cmp_lt_u32 s13, 62
	s_cbranch_scc1 .Lokw_53694
	s_waitcnt vmcnt(0)
.Lokw_53694:
	s_waitcnt vmcnt(7)
	s_add_i32 s14, s12, 1
	s_cmp_lg_u32 s12, 2
	s_cselect_b32 s12, s14, 0
	s_cmp_gt_u32 s13, 61
	s_mov_b32 s14, s13
	s_waitcnt vmcnt(7)
	v_cvt_pk_bf16_f32 v188, v188, v192
	v_cvt_pk_bf16_f32 v189, v189, v193
	v_cvt_pk_bf16_f32 v190, v190, v194
	v_cvt_pk_bf16_f32 v191, v191, v195
	ds_write_b128 v236, v[188:191]
	s_cbranch_scc0 .LBB0_3344
	s_waitcnt vmcnt(0)
	s_mov_b64 s[12:13], 0

.LBB0_3448:
	s_add_i32 s7, s8, 2
	s_add_i32 s8, s8, 4
	s_min_u32 s8, s8, 15
	s_mul_i32 s9, s6, 0xa000
	s_lshl_b32 s64, s8, 6
	s_add_i32 s24, s9, 0xffff6000
	s_cmp_lg_u32 s6, 0
	s_cselect_b32 s24, s24, 0x14000
	s_add_i32 s24, s22, s24
	s_waitcnt lgkmcnt(0)
	s_barrier
	s_cmp_lt_u32 s7, 14
	s_cbranch_scc0 .Lskipv_56180
	v_lshl_add_u64 v[156:157], v[200:201], 0, s[64:65]
	s_mov_b32 m0, s24
	s_nop 0
	global_load_lds_dwordx4 v[156:157], off
	v_lshl_add_u64 v[156:157], v[202:203], 0, s[64:65]
	s_add_i32 m0, s24, 0x400
	s_nop 0
	global_load_lds_dwordx4 v[156:157], off
	v_lshl_add_u64 v[156:157], v[204:205], 0, s[64:65]
	s_add_i32 m0, s24, 0x800
	s_nop 0
	global_load_lds_dwordx4 v[156:157], off
	v_lshl_add_u64 v[156:157], v[206:207], 0, s[64:65]
	s_add_i32 m0, s24, 0xc00
	s_nop 0
	global_load_lds_dwordx4 v[156:157], off
	v_lshl_add_u64 v[156:157], v[208:209], 0, s[64:65]
	s_add_i32 m0, s24, 0x1000
	s_lshl_b32 s64, s8, 18
	global_load_lds_dwordx4 v[156:157], off
	v_lshl_add_u64 v[156:157], v[210:211], 0, s[64:65]
	v_add_co_u32_e32 v160, vcc, s33, v156
	s_nop 1
	v_addc_co_u32_e32 v161, vcc, 0, v157, vcc
	global_load_dwordx4 v[156:159], v[156:157], off nt
	s_nop 0
	global_load_dwordx4 v[160:163], v[160:161], off nt
.Lskipv_56180:
	v_add_u32_e32 v167, s9, v86
	ds_read2_b32 v[168:169], v232 offset0:0 offset1:0x84
	ds_read2_b32 v[170:171], v233 offset0:0 offset1:0x84
	ds_read2_b32 v[172:173], v232 offset0:16 offset1:0x94
	ds_read2_b32 v[174:175], v233 offset0:16 offset1:0x94
	ds_read2_b32 v[176:177], v232 offset0:32 offset1:0xa4
	ds_read2_b32 v[178:179], v233 offset0:32 offset1:0xa4
	ds_read2_b32 v[180:181], v232 offset0:48 offset1:0xb4
	ds_read2_b32 v[182:183], v233 offset0:48 offset1:0xb4
	ds_read_b128 v[184:187], v167 offset:0
	ds_read_b128 v[188:191], v167 offset:0x400
	s_nop 0
	s_waitcnt lgkmcnt(1)
	s_setprio 1
	v_mfma_f32_16x16x32_bf16 v[78:81], v[168:171], v[184:187], v[78:81]
	v_mfma_f32_16x16x32_bf16 v[74:77], v[172:175], v[184:187], v[74:77]
	v_mfma_f32_16x16x32_bf16 v[70:73], v[176:179], v[184:187], v[70:73]
	v_mfma_f32_16x16x32_bf16 v[66:69], v[180:183], v[184:187], v[66:69]
	ds_read_b128 v[184:187], v167 offset:0x800
	s_waitcnt lgkmcnt(1)
	s_nop 0
	v_mfma_f32_16x16x32_bf16 v[62:65], v[168:171], v[188:191], v[62:65]
	v_mfma_f32_16x16x32_bf16 v[58:61], v[172:175], v[188:191], v[58:61]
	v_mfma_f32_16x16x32_bf16 v[54:57], v[176:179], v[188:191], v[54:57]
	v_mfma_f32_16x16x32_bf16 v[50:53], v[180:183], v[188:191], v[50:53]
	ds_read_b128 v[188:191], v167 offset:0xc00
	s_waitcnt lgkmcnt(1)
	s_nop 0
	v_mfma_f32_16x16x32_bf16 v[46:49], v[168:171], v[184:187], v[46:49]
	v_mfma_f32_16x16x32_bf16 v[42:45], v[172:175], v[184:187], v[42:45]
	v_mfma_f32_16x16x32_bf16 v[38:41], v[176:179], v[184:187], v[38:41]
	v_mfma_f32_16x16x32_bf16 v[34:37], v[180:183], v[184:187], v[34:37]
	ds_read_b128 v[184:187], v167 offset:0x1000
	s_waitcnt lgkmcnt(1)
	s_nop 0
	v_mfma_f32_16x16x32_bf16 v[18:21], v[168:171], v[188:191], v[18:21]
	v_mfma_f32_16x16x32_bf16 v[22:25], v[172:175], v[188:191], v[22:25]
	v_mfma_f32_16x16x32_bf16 v[26:29], v[176:179], v[188:191], v[26:29]
	v_mfma_f32_16x16x32_bf16 v[30:33], v[180:183], v[188:191], v[30:33]
	ds_read_b128 v[188:191], v167 offset:0x1400
	s_waitcnt lgkmcnt(1)
	s_nop 0
	v_mfma_f32_16x16x32_bf16 v[88:91], v[168:171], v[184:187], v[88:91]
	v_mfma_f32_16x16x32_bf16 v[112:115], v[172:175], v[184:187], v[112:115]
	v_mfma_f32_16x16x32_bf16 v[108:111], v[176:179], v[184:187], v[108:111]
	v_mfma_f32_16x16x32_bf16 v[100:103], v[180:183], v[184:187], v[100:103]
	ds_read_b128 v[184:187], v167 offset:0x1800
	s_waitcnt lgkmcnt(1)
	s_nop 0
	v_mfma_f32_16x16x32_bf16 v[82:85], v[168:171], v[188:191], v[82:85]
	v_mfma_f32_16x16x32_bf16 v[92:95], v[172:175], v[188:191], v[92:95]
	v_mfma_f32_16x16x32_bf16 v[96:99], v[176:179], v[188:191], v[96:99]
	v_mfma_f32_16x16x32_bf16 v[104:107], v[180:183], v[188:191], v[104:107]
	ds_read_b128 v[188:191], v167 offset:0x1c00
	s_waitcnt lgkmcnt(1)
	s_nop 0
	v_mfma_f32_16x16x32_bf16 v[116:119], v[168:171], v[184:187], v[116:119]
	s_waitcnt lgkmcnt(0)
	v_mfma_f32_16x16x32_bf16 v[124:127], v[172:175], v[184:187], v[124:127]
	v_mfma_f32_16x16x32_bf16 v[132:135], v[176:179], v[184:187], v[132:135]
	v_mfma_f32_16x16x32_bf16 v[136:139], v[180:183], v[184:187], v[136:139]
	v_mfma_f32_16x16x32_bf16 v[120:123], v[168:171], v[188:191], v[120:123]
	v_mfma_f32_16x16x32_bf16 v[128:131], v[172:175], v[188:191], v[128:131]
	v_mfma_f32_16x16x32_bf16 v[140:143], v[176:179], v[188:191], v[140:143]
	v_mfma_f32_16x16x32_bf16 v[144:147], v[180:183], v[188:191], v[144:147]
	s_setprio 0
	s_cmp_lt_u32 s7, 14
	s_cbranch_scc1 .Lokw_56180
	s_waitcnt vmcnt(0)
.Lokw_56180:
	s_add_i32 s8, s6, 1
	s_cmp_lg_u32 s6, 2
	s_cselect_b32 s6, s8, 0
	s_min_u32 s8, s7, 12
	s_add_i32 s8, s8, 3
	s_mul_i32 s9, s6, 0xa000
	s_lshl_b32 s64, s8, 6
	s_add_i32 s24, s9, 0xffff6000
	s_cmp_lg_u32 s6, 0
	s_waitcnt vmcnt(7)
	v_cvt_pk_bf16_f32 v148, v148, v152
	v_add_u32_e32 v152, 0x20100, v165
	s_cselect_b32 s24, s24, 0x14000
	v_cvt_pk_bf16_f32 v149, v149, v153
	v_cvt_pk_bf16_f32 v150, v150, v154
	v_cvt_pk_bf16_f32 v151, v151, v155
	ds_write_b128 v152, v[148:151]
	s_add_i32 s24, s22, s24
	s_waitcnt lgkmcnt(0)
	s_barrier
	s_cmp_lt_u32 s7, 14
	s_cbranch_scc0 .Lskipv_56354
	v_lshl_add_u64 v[148:149], v[200:201], 0, s[64:65]
	s_mov_b32 m0, s24
	s_nop 0
	global_load_lds_dwordx4 v[148:149], off
	v_lshl_add_u64 v[148:149], v[202:203], 0, s[64:65]
	s_add_i32 m0, s24, 0x400
	s_nop 0
	global_load_lds_dwordx4 v[148:149], off
	v_lshl_add_u64 v[148:149], v[204:205], 0, s[64:65]
	s_add_i32 m0, s24, 0x800
	s_nop 0
	global_load_lds_dwordx4 v[148:149], off
	v_lshl_add_u64 v[148:149], v[206:207], 0, s[64:65]
	s_add_i32 m0, s24, 0xc00
	s_nop 0
	global_load_lds_dwordx4 v[148:149], off
	v_lshl_add_u64 v[148:149], v[208:209], 0, s[64:65]
	s_lshl_b32 s64, s8, 18
	s_add_i32 m0, s24, 0x1000
	v_lshl_add_u64 v[152:153], v[210:211], 0, s[64:65]
	global_load_lds_dwordx4 v[148:149], off
	global_load_dwordx4 v[148:151], v[152:153], off nt
	v_add_co_u32_e32 v152, vcc, s33, v152
	s_nop 1
	v_addc_co_u32_e32 v153, vcc, 0, v153, vcc
	global_load_dwordx4 v[152:155], v[152:153], off nt
.Lskipv_56354:
	v_add_u32_e32 v167, s9, v86
	ds_read2_b32 v[168:169], v234 offset0:0 offset1:0x84
	ds_read2_b32 v[170:171], v235 offset0:0 offset1:0x84
	ds_read2_b32 v[172:173], v234 offset0:16 offset1:0x94
	ds_read2_b32 v[174:175], v235 offset0:16 offset1:0x94
	ds_read2_b32 v[176:177], v234 offset0:32 offset1:0xa4
	ds_read2_b32 v[178:179], v235 offset0:32 offset1:0xa4
	ds_read2_b32 v[180:181], v234 offset0:48 offset1:0xb4
	ds_read2_b32 v[182:183], v235 offset0:48 offset1:0xb4
	ds_read_b128 v[184:187], v167 offset:0
	ds_read_b128 v[188:191], v167 offset:0x400
	s_nop 0
	s_waitcnt lgkmcnt(1)
	s_setprio 1
	v_mfma_f32_16x16x32_bf16 v[78:81], v[168:171], v[184:187], v[78:81]
	v_mfma_f32_16x16x32_bf16 v[74:77], v[172:175], v[184:187], v[74:77]
	v_mfma_f32_16x16x32_bf16 v[70:73], v[176:179], v[184:187], v[70:73]
	v_mfma_f32_16x16x32_bf16 v[66:69], v[180:183], v[184:187], v[66:69]
	ds_read_b128 v[184:187], v167 offset:0x800
	s_waitcnt lgkmcnt(1)
	s_nop 0
	v_mfma_f32_16x16x32_bf16 v[62:65], v[168:171], v[188:191], v[62:65]
	v_mfma_f32_16x16x32_bf16 v[58:61], v[172:175], v[188:191], v[58:61]
	v_mfma_f32_16x16x32_bf16 v[54:57], v[176:179], v[188:191], v[54:57]
	v_mfma_f32_16x16x32_bf16 v[50:53], v[180:183], v[188:191], v[50:53]
	ds_read_b128 v[188:191], v167 offset:0xc00
	s_waitcnt lgkmcnt(1)
	s_nop 0
	v_mfma_f32_16x16x32_bf16 v[46:49], v[168:171], v[184:187], v[46:49]
	v_mfma_f32_16x16x32_bf16 v[42:45], v[172:175], v[184:187], v[42:45]
	v_mfma_f32_16x16x32_bf16 v[38:41], v[176:179], v[184:187], v[38:41]
	v_mfma_f32_16x16x32_bf16 v[34:37], v[180:183], v[184:187], v[34:37]
	ds_read_b128 v[184:187], v167 offset:0x1000
	s_waitcnt lgkmcnt(1)
	s_nop 0
	v_mfma_f32_16x16x32_bf16 v[18:21], v[168:171], v[188:191], v[18:21]
	v_mfma_f32_16x16x32_bf16 v[22:25], v[172:175], v[188:191], v[22:25]
	v_mfma_f32_16x16x32_bf16 v[26:29], v[176:179], v[188:191], v[26:29]
	v_mfma_f32_16x16x32_bf16 v[30:33], v[180:183], v[188:191], v[30:33]
	ds_read_b128 v[188:191], v167 offset:0x1400
	s_waitcnt lgkmcnt(1)
	s_nop 0
	v_mfma_f32_16x16x32_bf16 v[88:91], v[168:171], v[184:187], v[88:91]
	v_mfma_f32_16x16x32_bf16 v[112:115], v[172:175], v[184:187], v[112:115]
	v_mfma_f32_16x16x32_bf16 v[108:111], v[176:179], v[184:187], v[108:111]
	v_mfma_f32_16x16x32_bf16 v[100:103], v[180:183], v[184:187], v[100:103]
	ds_read_b128 v[184:187], v167 offset:0x1800
	s_waitcnt lgkmcnt(1)
	s_nop 0
	v_mfma_f32_16x16x32_bf16 v[82:85], v[168:171], v[188:191], v[82:85]
	v_mfma_f32_16x16x32_bf16 v[92:95], v[172:175], v[188:191], v[92:95]
	v_mfma_f32_16x16x32_bf16 v[96:99], v[176:179], v[188:191], v[96:99]
	v_mfma_f32_16x16x32_bf16 v[104:107], v[180:183], v[188:191], v[104:107]
	ds_read_b128 v[188:191], v167 offset:0x1c00
	s_waitcnt lgkmcnt(1)
	s_nop 0
	v_mfma_f32_16x16x32_bf16 v[116:119], v[168:171], v[184:187], v[116:119]
	s_waitcnt lgkmcnt(0)
	v_mfma_f32_16x16x32_bf16 v[124:127], v[172:175], v[184:187], v[124:127]
	v_mfma_f32_16x16x32_bf16 v[132:135], v[176:179], v[184:187], v[132:135]
	v_mfma_f32_16x16x32_bf16 v[136:139], v[180:183], v[184:187], v[136:139]
	v_mfma_f32_16x16x32_bf16 v[120:123], v[168:171], v[188:191], v[120:123]
	v_mfma_f32_16x16x32_bf16 v[128:131], v[172:175], v[188:191], v[128:131]
	v_mfma_f32_16x16x32_bf16 v[140:143], v[176:179], v[188:191], v[140:143]
	v_mfma_f32_16x16x32_bf16 v[144:147], v[180:183], v[188:191], v[144:147]
	s_setprio 0
	s_cmp_lt_u32 s7, 14
	s_cbranch_scc1 .Lokw_56354
	s_waitcnt vmcnt(0)
.Lokw_56354:
	s_waitcnt vmcnt(7)
	s_add_i32 s8, s6, 1
	s_cmp_lg_u32 s6, 2
	s_cselect_b32 s6, s8, 0
	s_cmp_gt_u32 s7, 13
	s_mov_b32 s8, s7
	s_waitcnt vmcnt(7)
	v_cvt_pk_bf16_f32 v156, v156, v160
	v_cvt_pk_bf16_f32 v157, v157, v161
	v_cvt_pk_bf16_f32 v158, v158, v162
	v_cvt_pk_bf16_f32 v159, v159, v163
	ds_write_b128 v166, v[156:159]
	s_cbranch_scc0 .LBB0_3448
	s_waitcnt vmcnt(0)
	s_mov_b64 s[6:7], 0
	s_branch .LBB0_3455

.LBB0_3466:
	s_add_i32 s5, s6, 2
	s_add_i32 s6, s6, 4
	s_min_u32 s6, s6, 15
	s_mul_i32 s7, s4, 0xa000
	s_lshl_b32 s64, s6, 6
	s_add_i32 s8, s7, 0xffff6000
	s_cmp_lg_u32 s4, 0
	s_cselect_b32 s8, s8, 0x14000
	s_add_i32 s8, s22, s8
	s_waitcnt lgkmcnt(0)
	s_barrier
	s_cmp_lt_u32 s5, 14
	s_cbranch_scc0 .Lskipv_57720
	v_lshl_add_u64 v[188:189], v[200:201], 0, s[64:65]
	s_mov_b32 m0, s8
	s_nop 0
	global_load_lds_dwordx4 v[188:189], off
	v_lshl_add_u64 v[188:189], v[202:203], 0, s[64:65]
	s_add_i32 m0, s8, 0x400
	s_nop 0
	global_load_lds_dwordx4 v[188:189], off
	v_lshl_add_u64 v[188:189], v[204:205], 0, s[64:65]
	s_add_i32 m0, s8, 0x800
	s_nop 0
	global_load_lds_dwordx4 v[188:189], off
	v_lshl_add_u64 v[188:189], v[206:207], 0, s[64:65]
	s_add_i32 m0, s8, 0xc00
	s_nop 0
	global_load_lds_dwordx4 v[188:189], off
	v_lshl_add_u64 v[188:189], v[208:209], 0, s[64:65]
	s_add_i32 m0, s8, 0x1000
	s_lshl_b32 s64, s6, 18
	global_load_lds_dwordx4 v[188:189], off
	v_lshl_add_u64 v[188:189], v[210:211], 0, s[64:65]
	v_add_co_u32_e32 v192, vcc, s33, v188
	s_nop 1
	v_addc_co_u32_e32 v193, vcc, 0, v189, vcc
	global_load_dwordx4 v[188:191], v[188:189], off nt
	s_nop 0
	global_load_dwordx4 v[192:195], v[192:193], off nt
.Lskipv_57720:
	v_add_u32_e32 v216, s7, v86
	ds_read2_b32 v[196:197], v232 offset0:0 offset1:0x84
	ds_read2_b32 v[198:199], v233 offset0:0 offset1:0x84
	ds_read2_b32 v[222:223], v232 offset0:16 offset1:0x94
	ds_read2_b32 v[224:225], v233 offset0:16 offset1:0x94
	ds_read2_b32 v[226:227], v232 offset0:32 offset1:0xa4
	ds_read2_b32 v[228:229], v233 offset0:32 offset1:0xa4
	ds_read2_b32 v[238:239], v232 offset0:48 offset1:0xb4
	ds_read2_b32 v[240:241], v233 offset0:48 offset1:0xb4
	ds_read_b128 v[242:245], v216 offset:0
	ds_read_b128 v[246:249], v216 offset:0x400
	s_nop 0
	s_waitcnt lgkmcnt(1)
	s_setprio 1
	v_mfma_f32_16x16x32_bf16 v[78:81], v[196:199], v[242:245], v[78:81]
	v_mfma_f32_16x16x32_bf16 v[74:77], v[222:225], v[242:245], v[74:77]
	v_mfma_f32_16x16x32_bf16 v[70:73], v[226:229], v[242:245], v[70:73]
	v_mfma_f32_16x16x32_bf16 v[66:69], v[238:241], v[242:245], v[66:69]
	ds_read_b128 v[242:245], v216 offset:0x800
	s_waitcnt lgkmcnt(1)
	s_nop 0
	v_mfma_f32_16x16x32_bf16 v[62:65], v[196:199], v[246:249], v[62:65]
	v_mfma_f32_16x16x32_bf16 v[58:61], v[222:225], v[246:249], v[58:61]
	v_mfma_f32_16x16x32_bf16 v[54:57], v[226:229], v[246:249], v[54:57]
	v_mfma_f32_16x16x32_bf16 v[50:53], v[238:241], v[246:249], v[50:53]
	ds_read_b128 v[246:249], v216 offset:0xc00
	s_waitcnt lgkmcnt(1)
	s_nop 0
	v_mfma_f32_16x16x32_bf16 v[46:49], v[196:199], v[242:245], v[46:49]
	v_mfma_f32_16x16x32_bf16 v[42:45], v[222:225], v[242:245], v[42:45]
	v_mfma_f32_16x16x32_bf16 v[38:41], v[226:229], v[242:245], v[38:41]
	v_mfma_f32_16x16x32_bf16 v[34:37], v[238:241], v[242:245], v[34:37]
	ds_read_b128 v[242:245], v216 offset:0x1000
	s_waitcnt lgkmcnt(1)
	s_nop 0
	v_mfma_f32_16x16x32_bf16 v[18:21], v[196:199], v[246:249], v[18:21]
	v_mfma_f32_16x16x32_bf16 v[22:25], v[222:225], v[246:249], v[22:25]
	v_mfma_f32_16x16x32_bf16 v[26:29], v[226:229], v[246:249], v[26:29]
	v_mfma_f32_16x16x32_bf16 v[30:33], v[238:241], v[246:249], v[30:33]
	ds_read_b128 v[246:249], v216 offset:0x1400
	s_waitcnt lgkmcnt(1)
	s_nop 0
	v_mfma_f32_16x16x32_bf16 v[88:91], v[196:199], v[242:245], v[88:91]
	v_mfma_f32_16x16x32_bf16 v[112:115], v[222:225], v[242:245], v[112:115]
	v_mfma_f32_16x16x32_bf16 v[108:111], v[226:229], v[242:245], v[108:111]
	v_mfma_f32_16x16x32_bf16 v[100:103], v[238:241], v[242:245], v[100:103]
	ds_read_b128 v[242:245], v216 offset:0x1800
	s_waitcnt lgkmcnt(1)
	s_nop 0
	v_mfma_f32_16x16x32_bf16 v[82:85], v[196:199], v[246:249], v[82:85]
	v_mfma_f32_16x16x32_bf16 v[92:95], v[222:225], v[246:249], v[92:95]
	v_mfma_f32_16x16x32_bf16 v[96:99], v[226:229], v[246:249], v[96:99]
	v_mfma_f32_16x16x32_bf16 v[104:107], v[238:241], v[246:249], v[104:107]
	ds_read_b128 v[246:249], v216 offset:0x1c00
	s_waitcnt lgkmcnt(1)
	s_nop 0
	v_mfma_f32_16x16x32_bf16 v[116:119], v[196:199], v[242:245], v[116:119]
	v_mfma_f32_16x16x32_bf16 v[124:127], v[222:225], v[242:245], v[124:127]
	v_mfma_f32_16x16x32_bf16 v[132:135], v[226:229], v[242:245], v[132:135]
	v_mfma_f32_16x16x32_bf16 v[136:139], v[238:241], v[242:245], v[136:139]
	ds_read_b128 v[242:245], v216 offset:0x2000
	s_waitcnt lgkmcnt(1)
	s_nop 0
	v_mfma_f32_16x16x32_bf16 v[120:123], v[196:199], v[246:249], v[120:123]
	v_mfma_f32_16x16x32_bf16 v[128:131], v[222:225], v[246:249], v[128:131]
	v_mfma_f32_16x16x32_bf16 v[140:143], v[226:229], v[246:249], v[140:143]
	v_mfma_f32_16x16x32_bf16 v[144:147], v[238:241], v[246:249], v[144:147]
	ds_read_b128 v[246:249], v216 offset:0x2400
	s_waitcnt lgkmcnt(1)
	s_nop 0
	v_mfma_f32_16x16x32_bf16 v[148:151], v[196:199], v[242:245], v[148:151]
	s_waitcnt lgkmcnt(0)
	v_mfma_f32_16x16x32_bf16 v[176:179], v[222:225], v[242:245], v[176:179]
	v_mfma_f32_16x16x32_bf16 v[172:175], v[226:229], v[242:245], v[172:175]
	v_mfma_f32_16x16x32_bf16 v[168:171], v[238:241], v[242:245], v[168:171]
	v_mfma_f32_16x16x32_bf16 v[164:167], v[196:199], v[246:249], v[164:167]
	v_mfma_f32_16x16x32_bf16 v[160:163], v[222:225], v[246:249], v[160:163]
	v_mfma_f32_16x16x32_bf16 v[156:159], v[226:229], v[246:249], v[156:159]
	v_mfma_f32_16x16x32_bf16 v[152:155], v[238:241], v[246:249], v[152:155]
	s_setprio 0
	s_cmp_lt_u32 s5, 14
	s_cbranch_scc1 .Lokw_57720
	s_waitcnt vmcnt(0)
.Lokw_57720:
	s_add_i32 s6, s4, 1
	s_cmp_lg_u32 s4, 2
	s_cselect_b32 s4, s6, 0
	s_min_u32 s6, s5, 12
	s_add_i32 s6, s6, 3
	s_mul_i32 s7, s4, 0xa000
	s_lshl_b32 s64, s6, 6
	s_add_i32 s8, s7, 0xffff6000
	s_cmp_lg_u32 s4, 0
	s_waitcnt vmcnt(7)
	v_cvt_pk_bf16_f32 v180, v180, v184
	v_add_u32_e32 v184, 0x20100, v236
	s_cselect_b32 s8, s8, 0x14000
	v_cvt_pk_bf16_f32 v181, v181, v185
	v_cvt_pk_bf16_f32 v182, v182, v186
	v_cvt_pk_bf16_f32 v183, v183, v187
	ds_write_b128 v184, v[180:183]
	s_add_i32 s8, s22, s8
	s_waitcnt lgkmcnt(0)
	s_barrier
	s_cmp_lt_u32 s5, 14
	s_cbranch_scc0 .Lskipv_57916
	v_lshl_add_u64 v[180:181], v[200:201], 0, s[64:65]
	s_mov_b32 m0, s8
	s_nop 0
	global_load_lds_dwordx4 v[180:181], off
	v_lshl_add_u64 v[180:181], v[202:203], 0, s[64:65]
	s_add_i32 m0, s8, 0x400
	s_nop 0
	global_load_lds_dwordx4 v[180:181], off
	v_lshl_add_u64 v[180:181], v[204:205], 0, s[64:65]
	s_add_i32 m0, s8, 0x800
	s_nop 0
	global_load_lds_dwordx4 v[180:181], off
	v_lshl_add_u64 v[180:181], v[206:207], 0, s[64:65]
	s_add_i32 m0, s8, 0xc00
	s_nop 0
	global_load_lds_dwordx4 v[180:181], off
	v_lshl_add_u64 v[180:181], v[208:209], 0, s[64:65]
	s_lshl_b32 s64, s6, 18
	s_add_i32 m0, s8, 0x1000
	v_lshl_add_u64 v[184:185], v[210:211], 0, s[64:65]
	global_load_lds_dwordx4 v[180:181], off
	global_load_dwordx4 v[180:183], v[184:185], off nt
	v_add_co_u32_e32 v184, vcc, s33, v184
	s_nop 1
	v_addc_co_u32_e32 v185, vcc, 0, v185, vcc
	global_load_dwordx4 v[184:187], v[184:185], off nt
.Lskipv_57916:
	v_add_u32_e32 v216, s7, v86
	ds_read2_b32 v[196:197], v234 offset0:0 offset1:0x84
	ds_read2_b32 v[198:199], v235 offset0:0 offset1:0x84
	ds_read2_b32 v[222:223], v234 offset0:16 offset1:0x94
	ds_read2_b32 v[224:225], v235 offset0:16 offset1:0x94
	ds_read2_b32 v[226:227], v234 offset0:32 offset1:0xa4
	ds_read2_b32 v[228:229], v235 offset0:32 offset1:0xa4
	ds_read2_b32 v[238:239], v234 offset0:48 offset1:0xb4
	ds_read2_b32 v[240:241], v235 offset0:48 offset1:0xb4
	ds_read_b128 v[242:245], v216 offset:0
	ds_read_b128 v[246:249], v216 offset:0x400
	s_nop 0
	s_waitcnt lgkmcnt(1)
	s_setprio 1
	v_mfma_f32_16x16x32_bf16 v[78:81], v[196:199], v[242:245], v[78:81]
	v_mfma_f32_16x16x32_bf16 v[74:77], v[222:225], v[242:245], v[74:77]
	v_mfma_f32_16x16x32_bf16 v[70:73], v[226:229], v[242:245], v[70:73]
	v_mfma_f32_16x16x32_bf16 v[66:69], v[238:241], v[242:245], v[66:69]
	ds_read_b128 v[242:245], v216 offset:0x800
	s_waitcnt lgkmcnt(1)
	s_nop 0
	v_mfma_f32_16x16x32_bf16 v[62:65], v[196:199], v[246:249], v[62:65]
	v_mfma_f32_16x16x32_bf16 v[58:61], v[222:225], v[246:249], v[58:61]
	v_mfma_f32_16x16x32_bf16 v[54:57], v[226:229], v[246:249], v[54:57]
	v_mfma_f32_16x16x32_bf16 v[50:53], v[238:241], v[246:249], v[50:53]
	ds_read_b128 v[246:249], v216 offset:0xc00
	s_waitcnt lgkmcnt(1)
	s_nop 0
	v_mfma_f32_16x16x32_bf16 v[46:49], v[196:199], v[242:245], v[46:49]
	v_mfma_f32_16x16x32_bf16 v[42:45], v[222:225], v[242:245], v[42:45]
	v_mfma_f32_16x16x32_bf16 v[38:41], v[226:229], v[242:245], v[38:41]
	v_mfma_f32_16x16x32_bf16 v[34:37], v[238:241], v[242:245], v[34:37]
	ds_read_b128 v[242:245], v216 offset:0x1000
	s_waitcnt lgkmcnt(1)
	s_nop 0
	v_mfma_f32_16x16x32_bf16 v[18:21], v[196:199], v[246:249], v[18:21]
	v_mfma_f32_16x16x32_bf16 v[22:25], v[222:225], v[246:249], v[22:25]
	v_mfma_f32_16x16x32_bf16 v[26:29], v[226:229], v[246:249], v[26:29]
	v_mfma_f32_16x16x32_bf16 v[30:33], v[238:241], v[246:249], v[30:33]
	ds_read_b128 v[246:249], v216 offset:0x1400
	s_waitcnt lgkmcnt(1)
	s_nop 0
	v_mfma_f32_16x16x32_bf16 v[88:91], v[196:199], v[242:245], v[88:91]
	v_mfma_f32_16x16x32_bf16 v[112:115], v[222:225], v[242:245], v[112:115]
	v_mfma_f32_16x16x32_bf16 v[108:111], v[226:229], v[242:245], v[108:111]
	v_mfma_f32_16x16x32_bf16 v[100:103], v[238:241], v[242:245], v[100:103]
	ds_read_b128 v[242:245], v216 offset:0x1800
	s_waitcnt lgkmcnt(1)
	s_nop 0
	v_mfma_f32_16x16x32_bf16 v[82:85], v[196:199], v[246:249], v[82:85]
	v_mfma_f32_16x16x32_bf16 v[92:95], v[222:225], v[246:249], v[92:95]
	v_mfma_f32_16x16x32_bf16 v[96:99], v[226:229], v[246:249], v[96:99]
	v_mfma_f32_16x16x32_bf16 v[104:107], v[238:241], v[246:249], v[104:107]
	ds_read_b128 v[246:249], v216 offset:0x1c00
	s_waitcnt lgkmcnt(1)
	s_nop 0
	v_mfma_f32_16x16x32_bf16 v[116:119], v[196:199], v[242:245], v[116:119]
	v_mfma_f32_16x16x32_bf16 v[124:127], v[222:225], v[242:245], v[124:127]
	v_mfma_f32_16x16x32_bf16 v[132:135], v[226:229], v[242:245], v[132:135]
	v_mfma_f32_16x16x32_bf16 v[136:139], v[238:241], v[242:245], v[136:139]
	ds_read_b128 v[242:245], v216 offset:0x2000
	s_waitcnt lgkmcnt(1)
	s_nop 0
	v_mfma_f32_16x16x32_bf16 v[120:123], v[196:199], v[246:249], v[120:123]
	v_mfma_f32_16x16x32_bf16 v[128:131], v[222:225], v[246:249], v[128:131]
	v_mfma_f32_16x16x32_bf16 v[140:143], v[226:229], v[246:249], v[140:143]
	v_mfma_f32_16x16x32_bf16 v[144:147], v[238:241], v[246:249], v[144:147]
	ds_read_b128 v[246:249], v216 offset:0x2400
	s_waitcnt lgkmcnt(1)
	s_nop 0
	v_mfma_f32_16x16x32_bf16 v[148:151], v[196:199], v[242:245], v[148:151]
	s_waitcnt lgkmcnt(0)
	v_mfma_f32_16x16x32_bf16 v[176:179], v[222:225], v[242:245], v[176:179]
	v_mfma_f32_16x16x32_bf16 v[172:175], v[226:229], v[242:245], v[172:175]
	v_mfma_f32_16x16x32_bf16 v[168:171], v[238:241], v[242:245], v[168:171]
	v_mfma_f32_16x16x32_bf16 v[164:167], v[196:199], v[246:249], v[164:167]
	v_mfma_f32_16x16x32_bf16 v[160:163], v[222:225], v[246:249], v[160:163]
	v_mfma_f32_16x16x32_bf16 v[156:159], v[226:229], v[246:249], v[156:159]
	v_mfma_f32_16x16x32_bf16 v[152:155], v[238:241], v[246:249], v[152:155]
	s_setprio 0
	s_cmp_lt_u32 s5, 14
	s_cbranch_scc1 .Lokw_57916
	s_waitcnt vmcnt(0)
.Lokw_57916:
	s_waitcnt vmcnt(7)
	s_add_i32 s6, s4, 1
	s_cmp_lg_u32 s4, 2
	s_cselect_b32 s4, s6, 0
	s_cmp_gt_u32 s5, 13
	s_mov_b32 s6, s5
	s_waitcnt vmcnt(7)
	v_cvt_pk_bf16_f32 v188, v188, v192
	v_cvt_pk_bf16_f32 v189, v189, v193
	v_cvt_pk_bf16_f32 v190, v190, v194
	v_cvt_pk_bf16_f32 v191, v191, v195
	ds_write_b128 v237, v[188:191]
	s_cbranch_scc0 .LBB0_3466
	s_waitcnt vmcnt(0)
	s_mov_b64 s[4:5], 0
